# phase G layer-0 out-proj epilogue: 12 of the second half's residual loads issued with the first half's (counted waits re-derived) (on v11)
# speedup vs baseline: 1.0051x; 1.0051x over previous
; __device__ __forceinline__ unsigned cvt_pk_bf16(float lo, float hi) { const f32x2 v = {lo, hi}; const bf16x2_t b = __builtin_convertvector(v, bf16x2_t); return __builtin_bit_cast(unsigned, b); }
;     __device__ __forceinline__ void operator()(AccRef acc, const Unit& u, int wr, int wc, int fr, int fq) const {
;         const int rr = u.pm < NLAT / 256 ? (u.pm >> 3) : 4; const int colb = u.pn * 256 + wc * 32 + 8 * fq;
;         const float* tb = (u.pm < NLAT / 256 ? xl + (size_t)(u.pm * 256) * DM : xc + (size_t)(u.pm * 256 - NLAT) * DM) + u.pn * 256;
;         const int lo = (wr * 64 + fr) * DM + wc * 32 + 8 * fq;
;         const float* gp = gate + (size_t)rr * 12288 + colb;
;         u32x4 pk[2][4][2];
;         { const f32x4 g00 = *(const f32x4*)gp, g01 = *(const f32x4*)(gp + 4), g10 = *(const f32x4*)(gp + 128), g11 = *(const f32x4*)(gp + 132);
; #pragma unroll
;           for (int ai = 0; ai < 2; ++ai)
; #pragma unroll
;             for (int m = 0; m < 4; ++m)
; #pragma unroll
;                 for (int bj = 0; bj < 2; ++bj) { const f32x4 y0 = (bj ? g10 : g00) * acc[ai][bj][m][0], y1 = (bj ? g11 : g01) * acc[ai][bj][m][1];
;                     pk[ai][m][bj].x = cvt_pk_bf16(y0[0], y0[1]); pk[ai][m][bj].y = cvt_pk_bf16(y0[2], y0[3]); pk[ai][m][bj].z = cvt_pk_bf16(y1[0], y1[1]); pk[ai][m][bj].w = cvt_pk_bf16(y1[2], y1[3]); } }
;         asm volatile("" ::: "memory");
; #pragma unroll
;         for (int ai = 0; ai < 2; ++ai) {
;             f32x4 xa[4][2][2];
; #pragma unroll
;             for (int m = 0; m < 4; ++m)
; #pragma unroll
;                 for (int bj = 0; bj < 2; ++bj) { const float* src = tb + (lo + (ai * 128 + m * 16) * DM + bj * 128); xa[m][bj][0] = *(const f32x4*)src; xa[m][bj][1] = *(const f32x4*)(src + 4); }
.LBB0_1675:
	s_lshl_b32 s14, s48, 8
	s_add_i32 s15, s14, 0xffffe000
	s_ashr_i32 s16, s14, 31
	s_and_b64 s[0:1], s[0:1], exec
	s_cselect_b32 s1, s16, 0
	s_cselect_b32 s0, s14, s15
	s_lshl_b64 s[0:1], s[0:1], 13
	s_add_u32 s15, s24, s0
	s_addc_u32 s16, s25, s1
	s_lshl_b32 s0, s63, 8
	s_ashr_i32 s1, s0, 31
	s_lshl_b64 s[12:13], s[12:13], 2
	v_or_b32_e32 v158, s0, v162
	s_add_u32 s12, s55, s12
	s_addc_u32 s13, s56, s13
	v_ashrrev_i32_e32 v159, 31, v158
	v_lshl_add_u64 v[176:177], v[158:159], 2, s[12:13]
	global_load_dwordx4 v[164:167], v[176:177], off offset:16
	global_load_dwordx4 v[168:171], v[176:177], off
	global_load_dwordx4 v[172:175], v[176:177], off offset:528
	s_nop 0
	global_load_dwordx4 v[176:179], v[176:177], off offset:512
	s_lshl_b64 s[0:1], s[0:1], 2
	s_add_u32 s24, s15, s0
	s_addc_u32 s25, s16, s1
	s_mov_b64 s[0:1], 0x20000
	v_readlane_b32 s94, v251, 63
	s_waitcnt vmcnt(0)
	v_pk_mul_f32 v[180:181], v[124:125], v[166:167]
	v_pk_mul_f32 v[126:127], v[126:127], v[168:169]
	v_pk_mul_f32 v[108:109], v[108:109], v[174:175]
	v_pk_mul_f32 v[110:111], v[110:111], v[176:177]
	v_pk_mul_f32 v[106:107], v[106:107], v[172:173]
	v_cvt_pk_bf16_f32 v125, v126, v127
	v_pk_mul_f32 v[126:127], v[112:113], v[178:179]
	v_cvt_pk_bf16_f32 v113, v110, v111
	v_cvt_pk_bf16_f32 v111, v106, v107
	v_cvt_pk_bf16_f32 v110, v108, v109
	v_pk_mul_f32 v[106:107], v[120:121], v[170:171]
	v_pk_mul_f32 v[108:109], v[118:119], v[168:169]
	v_pk_mul_f32 v[114:115], v[114:115], v[164:165]
	v_pk_mul_f32 v[94:95], v[94:95], v[176:177]
	v_pk_mul_f32 v[92:93], v[92:93], v[174:175]
	v_pk_mul_f32 v[90:91], v[90:91], v[172:173]
	v_cvt_pk_bf16_f32 v109, v108, v109
	v_cvt_pk_bf16_f32 v108, v106, v107
	v_cvt_pk_bf16_f32 v107, v114, v115
	v_pk_mul_f32 v[114:115], v[96:97], v[178:179]
	v_cvt_pk_bf16_f32 v97, v94, v95
	v_cvt_pk_bf16_f32 v95, v90, v91
	v_cvt_pk_bf16_f32 v94, v92, v93
	v_pk_mul_f32 v[90:91], v[104:105], v[170:171]
	v_pk_mul_f32 v[92:93], v[102:103], v[168:169]
	v_pk_mul_f32 v[98:99], v[98:99], v[164:165]
	v_pk_mul_f32 v[78:79], v[78:79], v[176:177]
	v_pk_mul_f32 v[76:77], v[76:77], v[174:175]
	v_pk_mul_f32 v[74:75], v[74:75], v[172:173]
	v_cvt_pk_bf16_f32 v93, v92, v93
	v_cvt_pk_bf16_f32 v92, v90, v91
	v_cvt_pk_bf16_f32 v91, v98, v99
	v_pk_mul_f32 v[98:99], v[80:81], v[178:179]
	v_cvt_pk_bf16_f32 v81, v78, v79
	v_cvt_pk_bf16_f32 v79, v74, v75
	v_cvt_pk_bf16_f32 v78, v76, v77
	v_pk_mul_f32 v[74:75], v[88:89], v[170:171]
	v_pk_mul_f32 v[76:77], v[86:87], v[168:169]
	v_pk_mul_f32 v[82:83], v[82:83], v[164:165]
	v_pk_mul_f32 v[70:71], v[70:71], v[176:177]
	v_pk_mul_f32 v[62:63], v[62:63], v[168:169]
	v_pk_mul_f32 v[58:59], v[58:59], v[164:165]
	v_pk_mul_f32 v[44:45], v[44:45], v[174:175]
	v_pk_mul_f32 v[42:43], v[42:43], v[172:173]
	v_cvt_pk_bf16_f32 v77, v76, v77
	v_cvt_pk_bf16_f32 v76, v74, v75
	v_cvt_pk_bf16_f32 v75, v82, v83
	v_pk_mul_f32 v[82:83], v[68:69], v[174:175]
	v_cvt_pk_bf16_f32 v69, v70, v71
	v_pk_mul_f32 v[70:71], v[64:65], v[170:171]
	v_cvt_pk_bf16_f32 v65, v62, v63
	v_cvt_pk_bf16_f32 v63, v58, v59
	v_cvt_pk_bf16_f32 v59, v42, v43
	v_cvt_pk_bf16_f32 v58, v44, v45
	v_pk_mul_f32 v[42:43], v[56:57], v[170:171]
	v_pk_mul_f32 v[44:45], v[54:55], v[168:169]
	v_pk_mul_f32 v[16:17], v[16:17], v[178:179]
	v_pk_mul_f32 v[14:15], v[14:15], v[176:177]
	v_pk_mul_f32 v[12:13], v[12:13], v[174:175]
	v_pk_mul_f32 v[10:11], v[10:11], v[172:173]
	v_pk_mul_f32 v[60:61], v[60:61], v[166:167]
	v_pk_mul_f32 v[48:49], v[48:49], v[178:179]
	v_pk_mul_f32 v[46:47], v[46:47], v[176:177]
	v_cvt_pk_bf16_f32 v57, v44, v45
	v_cvt_pk_bf16_f32 v56, v42, v43
	v_pk_mul_f32 v[32:33], v[32:33], v[178:179]
	v_pk_mul_f32 v[30:31], v[30:31], v[176:177]
	v_pk_mul_f32 v[28:29], v[28:29], v[174:175]
	v_pk_mul_f32 v[26:27], v[26:27], v[172:173]
	v_cvt_pk_bf16_f32 v45, v14, v15
	v_cvt_pk_bf16_f32 v44, v16, v17
	v_cvt_pk_bf16_f32 v43, v10, v11
	v_cvt_pk_bf16_f32 v42, v12, v13
	v_pk_mul_f32 v[10:11], v[24:25], v[170:171]
	v_pk_mul_f32 v[12:13], v[22:23], v[168:169]
	v_pk_mul_f32 v[14:15], v[20:21], v[166:167]
	v_pk_mul_f32 v[16:17], v[18:19], v[164:165]
	v_pk_mul_f32 v[8:9], v[8:9], v[178:179]
	v_pk_mul_f32 v[6:7], v[6:7], v[176:177]
	v_pk_mul_f32 v[4:5], v[4:5], v[174:175]
	v_pk_mul_f32 v[2:3], v[2:3], v[172:173]
	v_lshl_add_u64 v[18:19], v[136:137], 2, s[24:25]
	v_cvt_pk_bf16_f32 v62, v60, v61
	v_cvt_pk_bf16_f32 v61, v46, v47
	v_cvt_pk_bf16_f32 v60, v48, v49
	v_pk_mul_f32 v[46:47], v[52:53], v[166:167]
	v_pk_mul_f32 v[48:49], v[50:51], v[164:165]
	v_cvt_pk_bf16_f32 v53, v30, v31
	v_cvt_pk_bf16_f32 v52, v32, v33
	v_cvt_pk_bf16_f32 v51, v26, v27
	v_cvt_pk_bf16_f32 v50, v28, v29
	v_pk_mul_f32 v[26:27], v[40:41], v[170:171]
	v_pk_mul_f32 v[28:29], v[38:39], v[168:169]
	v_pk_mul_f32 v[30:31], v[36:37], v[166:167]
	v_pk_mul_f32 v[32:33], v[34:35], v[164:165]
	v_cvt_pk_bf16_f32 v41, v12, v13
	v_cvt_pk_bf16_f32 v40, v10, v11
	v_cvt_pk_bf16_f32 v39, v16, v17
	v_cvt_pk_bf16_f32 v38, v14, v15
	v_cvt_pk_bf16_f32 v37, v6, v7
	v_cvt_pk_bf16_f32 v36, v8, v9
	v_cvt_pk_bf16_f32 v35, v2, v3
	v_cvt_pk_bf16_f32 v34, v4, v5
	global_load_dwordx4 v[2:5], v[18:19], off offset:16
	global_load_dwordx4 v[6:9], v[18:19], off
	global_load_dwordx4 v[10:13], v[18:19], off offset:528
	global_load_dwordx4 v[14:17], v[18:19], off offset:512
	v_lshl_add_u64 v[20:21], v[18:19], 0, s[0:1]
	s_mov_b32 s0, 0x20000
	v_add_co_u32_e32 v22, vcc, s0, v18
	v_pk_mul_f32 v[84:85], v[84:85], v[166:167]
	v_pk_mul_f32 v[72:73], v[72:73], v[178:179]
	v_pk_mul_f32 v[66:67], v[66:67], v[172:173]
	v_addc_co_u32_e32 v23, vcc, 0, v19, vcc
	v_cvt_pk_bf16_f32 v74, v84, v85
	v_cvt_pk_bf16_f32 v68, v72, v73
	v_cvt_pk_bf16_f32 v67, v66, v67
; __device__ __forceinline__ unsigned cvt_pk_bf16(float lo, float hi) { const f32x2 v = {lo, hi}; const bf16x2_t b = __builtin_convertvector(v, bf16x2_t); return __builtin_bit_cast(unsigned, b); }
; __device__ __forceinline__ float bflo(unsigned w) { return __uint_as_float(w << 16); }
; __device__ __forceinline__ float bfhi(unsigned w) { return __uint_as_float(w & 0xffff0000u); }
;     __device__ __forceinline__ void operator()(AccRef acc, const Unit& u, int wr, int wc, int fr, int fq) const {
;     ...
;                 for (int bj = 0; bj < 2; ++bj) { const float* src = tb + (lo + (ai * 128 + m * 16) * DM + bj * 128); xa[m][bj][0] = *(const f32x4*)src; xa[m][bj][1] = *(const f32x4*)(src + 4); }
; #pragma unroll
;             for (int m = 0; m < 4; ++m)
; #pragma unroll
;                 for (int bj = 0; bj < 2; ++bj) { const int row = u.pm * 256 + ai * 128 + wr * 64 + m * 16 + fr, col = colb + bj * 128; const u32x4 y = pk[ai][m][bj];
;                     const f32x4 x0 = xa[m][bj][0] + (f32x4){bflo(y.x), bfhi(y.x), bflo(y.y), bfhi(y.y)}, x1 = xa[m][bj][1] + (f32x4){bflo(y.z), bfhi(y.z), bflo(y.w), bfhi(y.w)};
;                     u32x4 w; w.x = cvt_pk_bf16(x0[0], x0[1]); w.y = cvt_pk_bf16(x0[2], x0[3]); w.z = cvt_pk_bf16(x1[0], x1[1]); w.w = cvt_pk_bf16(x1[2], x1[3]);
;                     *(u32x4*)(xo + (size_t)row * DM + col) = w; }
	v_cvt_pk_bf16_f32 v66, v82, v83
	v_cvt_pk_bf16_f32 v64, v70, v71
	global_load_dwordx4 v[70:73], v[22:23], off
	global_load_dwordx4 v[82:85], v[20:21], off offset:16
	v_pk_mul_f32 v[100:101], v[100:101], v[166:167]
	s_mov_b64 s[0:1], 0x20200
	v_cvt_pk_bf16_f32 v90, v100, v101
	v_cvt_pk_bf16_f32 v80, v98, v99
	v_lshl_add_u64 v[20:21], v[18:19], 0, s[0:1]
	global_load_dwordx4 v[86:89], v[22:23], off offset:512
	global_load_dwordx4 v[98:101], v[20:21], off offset:16
	s_mov_b64 s[0:1], 0x40000
	v_lshl_add_u64 v[20:21], v[18:19], 0, s[0:1]
	s_mov_b32 s0, 0x40000
	v_add_co_u32_e32 v22, vcc, s0, v18
	v_pk_mul_f32 v[116:117], v[116:117], v[166:167]
	s_nop 0
	v_addc_co_u32_e32 v23, vcc, 0, v19, vcc
	v_cvt_pk_bf16_f32 v106, v116, v117
	v_cvt_pk_bf16_f32 v96, v114, v115
	global_load_dwordx4 v[102:105], v[22:23], off
	global_load_dwordx4 v[114:117], v[20:21], off offset:16
	v_pk_mul_f32 v[128:129], v[128:129], v[170:171]
	s_mov_b64 s[0:1], 0x40200
	v_cvt_pk_bf16_f32 v124, v128, v129
	v_cvt_pk_bf16_f32 v112, v126, v127
	v_lshl_add_u64 v[20:21], v[18:19], 0, s[0:1]
	global_load_dwordx4 v[118:121], v[22:23], off offset:512
	global_load_dwordx4 v[126:129], v[20:21], off offset:16
	s_mov_b64 s[0:1], 0x60000
	v_lshl_add_u64 v[20:21], v[18:19], 0, s[0:1]
	s_mov_b32 s0, 0x60000
	v_add_co_u32_e32 v22, vcc, s0, v18
	v_pk_mul_f32 v[122:123], v[122:123], v[164:165]
	s_nop 0
	v_addc_co_u32_e32 v23, vcc, 0, v19, vcc
	v_cvt_pk_bf16_f32 v55, v48, v49
	v_cvt_pk_bf16_f32 v49, v28, v29
	v_cvt_pk_bf16_f32 v48, v26, v27
	global_load_dwordx4 v[164:167], v[22:23], off
	global_load_dwordx4 v[26:29], v[20:21], off offset:16
	s_mov_b64 s[0:1], 0x60200
	v_lshl_add_u64 v[18:19], v[18:19], 0, s[0:1]
	global_load_dwordx4 v[22:25], v[22:23], off offset:512
	s_nop 0
	global_load_dwordx4 v[18:21], v[18:19], off offset:16
	v_lshl_add_u64 v[186:187], v[138:139], 2, s[24:25]
	global_load_dwordx4 v[182:185], v[186:187], off offset:16
	s_nop 0
	global_load_dwordx4 v[186:189], v[186:187], off
	v_lshl_add_u64 v[194:195], v[140:141], 2, s[24:25]
	global_load_dwordx4 v[190:193], v[194:195], off offset:16
	s_nop 0
	global_load_dwordx4 v[194:197], v[194:195], off
	v_lshl_add_u64 v[202:203], v[142:143], 2, s[24:25]
	global_load_dwordx4 v[198:201], v[202:203], off offset:16
	s_nop 0
	global_load_dwordx4 v[202:205], v[202:203], off
	v_lshl_add_u64 v[220:221], v[144:145], 2, s[24:25]
	global_load_dwordx4 v[216:219], v[220:221], off offset:16
	s_nop 0
	global_load_dwordx4 v[220:223], v[220:221], off
	v_lshl_add_u64 v[228:229], v[146:147], 2, s[24:25]
	global_load_dwordx4 v[224:227], v[228:229], off offset:16
	s_nop 0
	global_load_dwordx4 v[228:231], v[228:229], off
	v_lshl_add_u64 v[236:237], v[148:149], 2, s[24:25]
	global_load_dwordx4 v[232:235], v[236:237], off offset:16
	s_nop 0
	global_load_dwordx4 v[236:239], v[236:237], off
	v_cvt_pk_bf16_f32 v54, v46, v47
	v_cvt_pk_bf16_f32 v46, v30, v31
	v_add_u32_e32 v30, s14, v160
	v_cvt_pk_bf16_f32 v123, v122, v123
	v_cvt_pk_bf16_f32 v122, v180, v181
	v_ashrrev_i32_e32 v31, 31, v30
	v_lshlrev_b32_e32 v168, 16, v125
	v_and_b32_e32 v169, 0xffff0000, v125
	v_readlane_b32 s0, v253, 53
	v_cvt_pk_bf16_f32 v47, v32, v33
	v_lshlrev_b64 v[32:33], 12, v[30:31]
	v_lshlrev_b32_e32 v170, 16, v124
	v_and_b32_e32 v171, 0xffff0000, v124
	v_lshlrev_b32_e32 v124, 16, v123
	v_and_b32_e32 v125, 0xffff0000, v123
	v_readlane_b32 s1, v253, 54
	s_andn2_b64 vcc, exec, s[36:37]
	s_waitcnt vmcnt(26)
	v_pk_add_f32 v[6:7], v[6:7], v[168:169]
	v_lshlrev_b32_e32 v168, 16, v122
	v_and_b32_e32 v169, 0xffff0000, v122
	v_pk_add_f32 v[8:9], v[8:9], v[170:171]
	v_pk_add_f32 v[122:123], v[4:5], v[168:169]
	v_pk_add_f32 v[4:5], v[2:3], v[124:125]
	v_cvt_pk_bf16_f32 v2, v6, v7
	v_lshl_add_u64 v[6:7], s[0:1], 0, v[32:33]
	v_lshlrev_b64 v[32:33], 1, v[158:159]
	v_cvt_pk_bf16_f32 v3, v8, v9
	v_cvt_pk_bf16_f32 v4, v4, v5
	v_cvt_pk_bf16_f32 v5, v122, v123
	v_lshl_add_u64 v[6:7], v[6:7], 0, v[32:33]
	global_store_dwordx4 v[6:7], v[2:5], off
	v_lshlrev_b32_e32 v8, 16, v111
	v_and_b32_e32 v9, 0xffff0000, v111
	v_lshlrev_b32_e32 v2, 16, v113
	v_and_b32_e32 v3, 0xffff0000, v113
	v_lshlrev_b32_e32 v4, 16, v112
	v_and_b32_e32 v5, 0xffff0000, v112
	s_waitcnt vmcnt(25)
	v_pk_add_f32 v[2:3], v[14:15], v[2:3]
	v_lshlrev_b32_e32 v14, 16, v110
	v_and_b32_e32 v15, 0xffff0000, v110
	v_pk_add_f32 v[4:5], v[16:17], v[4:5]
	v_pk_add_f32 v[12:13], v[12:13], v[14:15]
	v_pk_add_f32 v[8:9], v[10:11], v[8:9]
	v_cvt_pk_bf16_f32 v2, v2, v3
	v_cvt_pk_bf16_f32 v3, v4, v5
	v_cvt_pk_bf16_f32 v4, v8, v9
	v_cvt_pk_bf16_f32 v5, v12, v13
	global_store_dwordx4 v[6:7], v[2:5], off offset:256
	v_lshlrev_b32_e32 v8, 16, v107
	v_and_b32_e32 v9, 0xffff0000, v107
	v_or_b32_e32 v2, 16, v30
	v_ashrrev_i32_e32 v3, 31, v2
	v_lshlrev_b64 v[6:7], 12, v[2:3]
	v_lshlrev_b32_e32 v2, 16, v109
	v_and_b32_e32 v3, 0xffff0000, v109
	v_lshlrev_b32_e32 v4, 16, v108
	v_and_b32_e32 v5, 0xffff0000, v108
	v_lshlrev_b32_e32 v10, 16, v106
	v_and_b32_e32 v11, 0xffff0000, v106
	s_waitcnt vmcnt(25)
	v_pk_add_f32 v[4:5], v[72:73], v[4:5]
	v_pk_add_f32 v[2:3], v[70:71], v[2:3]
	s_waitcnt vmcnt(24)
	v_pk_add_f32 v[10:11], v[84:85], v[10:11]
	v_pk_add_f32 v[8:9], v[82:83], v[8:9]
	v_lshl_add_u64 v[6:7], s[0:1], 0, v[6:7]
	v_cvt_pk_bf16_f32 v2, v2, v3
	v_cvt_pk_bf16_f32 v3, v4, v5
	v_cvt_pk_bf16_f32 v4, v8, v9
	v_cvt_pk_bf16_f32 v5, v10, v11
	v_lshl_add_u64 v[6:7], v[6:7], 0, v[32:33]
	global_store_dwordx4 v[6:7], v[2:5], off
	v_lshlrev_b32_e32 v8, 16, v95
	v_and_b32_e32 v9, 0xffff0000, v95
	v_lshlrev_b32_e32 v2, 16, v97
	v_and_b32_e32 v3, 0xffff0000, v97
	v_lshlrev_b32_e32 v4, 16, v96
	v_and_b32_e32 v5, 0xffff0000, v96
	v_lshlrev_b32_e32 v10, 16, v94
	v_and_b32_e32 v11, 0xffff0000, v94
	s_waitcnt vmcnt(24)
; __device__ __forceinline__ unsigned cvt_pk_bf16(float lo, float hi) { const f32x2 v = {lo, hi}; const bf16x2_t b = __builtin_convertvector(v, bf16x2_t); return __builtin_bit_cast(unsigned, b); }
; __device__ __forceinline__ float bflo(unsigned w) { return __uint_as_float(w << 16); }
; __device__ __forceinline__ float bfhi(unsigned w) { return __uint_as_float(w & 0xffff0000u); }
;     __device__ __forceinline__ void operator()(AccRef acc, const Unit& u, int wr, int wc, int fr, int fq) const {
;     ...
; #pragma unroll
;         for (int ai = 0; ai < 2; ++ai) {
;             f32x4 xa[4][2][2];
; #pragma unroll
;             for (int m = 0; m < 4; ++m)
; #pragma unroll
;                 for (int bj = 0; bj < 2; ++bj) { const float* src = tb + (lo + (ai * 128 + m * 16) * DM + bj * 128); xa[m][bj][0] = *(const f32x4*)src; xa[m][bj][1] = *(const f32x4*)(src + 4); }
; #pragma unroll
;             for (int m = 0; m < 4; ++m)
; #pragma unroll
;                 for (int bj = 0; bj < 2; ++bj) { const int row = u.pm * 256 + ai * 128 + wr * 64 + m * 16 + fr, col = colb + bj * 128; const u32x4 y = pk[ai][m][bj];
;                     const f32x4 x0 = xa[m][bj][0] + (f32x4){bflo(y.x), bfhi(y.x), bflo(y.y), bfhi(y.y)}, x1 = xa[m][bj][1] + (f32x4){bflo(y.z), bfhi(y.z), bflo(y.w), bfhi(y.w)};
;                     u32x4 w; w.x = cvt_pk_bf16(x0[0], x0[1]); w.y = cvt_pk_bf16(x0[2], x0[3]); w.z = cvt_pk_bf16(x1[0], x1[1]); w.w = cvt_pk_bf16(x1[2], x1[3]);
;                     *(u32x4*)(xo + (size_t)row * DM + col) = w; }
	v_pk_add_f32 v[4:5], v[88:89], v[4:5]
	v_pk_add_f32 v[2:3], v[86:87], v[2:3]
	s_waitcnt vmcnt(23)
	v_pk_add_f32 v[10:11], v[100:101], v[10:11]
	v_pk_add_f32 v[8:9], v[98:99], v[8:9]
	v_cvt_pk_bf16_f32 v2, v2, v3
	v_cvt_pk_bf16_f32 v3, v4, v5
	v_cvt_pk_bf16_f32 v4, v8, v9
	v_cvt_pk_bf16_f32 v5, v10, v11
	global_store_dwordx4 v[6:7], v[2:5], off offset:256
	v_lshlrev_b32_e32 v8, 16, v91
	v_and_b32_e32 v9, 0xffff0000, v91
	v_or_b32_e32 v2, 32, v30
	v_ashrrev_i32_e32 v3, 31, v2
	v_lshlrev_b64 v[6:7], 12, v[2:3]
	v_lshlrev_b32_e32 v2, 16, v93
	v_and_b32_e32 v3, 0xffff0000, v93
	v_lshlrev_b32_e32 v4, 16, v92
	v_and_b32_e32 v5, 0xffff0000, v92
	v_lshlrev_b32_e32 v10, 16, v90
	v_and_b32_e32 v11, 0xffff0000, v90
	s_waitcnt vmcnt(23)
	v_pk_add_f32 v[4:5], v[104:105], v[4:5]
	v_pk_add_f32 v[2:3], v[102:103], v[2:3]
	s_waitcnt vmcnt(22)
	v_pk_add_f32 v[10:11], v[116:117], v[10:11]
	v_pk_add_f32 v[8:9], v[114:115], v[8:9]
	v_lshl_add_u64 v[6:7], s[0:1], 0, v[6:7]
	v_cvt_pk_bf16_f32 v2, v2, v3
	v_cvt_pk_bf16_f32 v3, v4, v5
	v_cvt_pk_bf16_f32 v4, v8, v9
	v_cvt_pk_bf16_f32 v5, v10, v11
	v_lshl_add_u64 v[6:7], v[6:7], 0, v[32:33]
	global_store_dwordx4 v[6:7], v[2:5], off
	v_lshlrev_b32_e32 v8, 16, v79
	v_and_b32_e32 v9, 0xffff0000, v79
	v_lshlrev_b32_e32 v2, 16, v81
	v_and_b32_e32 v3, 0xffff0000, v81
	v_lshlrev_b32_e32 v4, 16, v80
	v_and_b32_e32 v5, 0xffff0000, v80
	v_lshlrev_b32_e32 v10, 16, v78
	v_and_b32_e32 v11, 0xffff0000, v78
	s_waitcnt vmcnt(22)
	v_pk_add_f32 v[4:5], v[120:121], v[4:5]
	v_pk_add_f32 v[2:3], v[118:119], v[2:3]
	s_waitcnt vmcnt(21)
	v_pk_add_f32 v[10:11], v[128:129], v[10:11]
	v_pk_add_f32 v[8:9], v[126:127], v[8:9]
	v_cvt_pk_bf16_f32 v2, v2, v3
	v_cvt_pk_bf16_f32 v3, v4, v5
	v_cvt_pk_bf16_f32 v4, v8, v9
	v_cvt_pk_bf16_f32 v5, v10, v11
	global_store_dwordx4 v[6:7], v[2:5], off offset:256
	v_lshlrev_b32_e32 v8, 16, v75
	v_and_b32_e32 v9, 0xffff0000, v75
	v_or_b32_e32 v2, 48, v30
	v_ashrrev_i32_e32 v3, 31, v2
	v_lshlrev_b64 v[6:7], 12, v[2:3]
	v_lshlrev_b32_e32 v2, 16, v77
	v_and_b32_e32 v3, 0xffff0000, v77
	v_lshlrev_b32_e32 v4, 16, v76
	v_and_b32_e32 v5, 0xffff0000, v76
	v_lshlrev_b32_e32 v10, 16, v74
	v_and_b32_e32 v11, 0xffff0000, v74
	s_waitcnt vmcnt(21)
	v_pk_add_f32 v[4:5], v[166:167], v[4:5]
	v_pk_add_f32 v[2:3], v[164:165], v[2:3]
	s_waitcnt vmcnt(20)
	v_pk_add_f32 v[10:11], v[28:29], v[10:11]
	v_pk_add_f32 v[8:9], v[26:27], v[8:9]
	v_lshl_add_u64 v[6:7], s[0:1], 0, v[6:7]
	v_cvt_pk_bf16_f32 v2, v2, v3
	v_cvt_pk_bf16_f32 v3, v4, v5
	v_cvt_pk_bf16_f32 v4, v8, v9
	v_cvt_pk_bf16_f32 v5, v10, v11
	v_lshl_add_u64 v[6:7], v[6:7], 0, v[32:33]
	global_store_dwordx4 v[6:7], v[2:5], off
	v_lshlrev_b32_e32 v8, 16, v67
	v_and_b32_e32 v9, 0xffff0000, v67
	v_lshlrev_b32_e32 v2, 16, v69
	v_and_b32_e32 v3, 0xffff0000, v69
	v_lshlrev_b32_e32 v4, 16, v68
	v_and_b32_e32 v5, 0xffff0000, v68
	v_lshlrev_b32_e32 v10, 16, v66
	v_and_b32_e32 v11, 0xffff0000, v66
	s_waitcnt vmcnt(20)
	v_pk_add_f32 v[4:5], v[24:25], v[4:5]
	v_pk_add_f32 v[2:3], v[22:23], v[2:3]
	s_waitcnt vmcnt(19)
	v_pk_add_f32 v[10:11], v[20:21], v[10:11]
	v_pk_add_f32 v[8:9], v[18:19], v[8:9]
	v_cvt_pk_bf16_f32 v2, v2, v3
	v_cvt_pk_bf16_f32 v3, v4, v5
	v_cvt_pk_bf16_f32 v4, v8, v9
	v_cvt_pk_bf16_f32 v5, v10, v11
	global_store_dwordx4 v[6:7], v[2:5], off offset:256
	v_lshl_add_u64 v[6:7], v[152:153], 2, s[24:25]
	v_add_u32_e32 v102, 0x80, v30
	v_lshl_add_u64 v[2:3], v[150:151], 2, s[24:25]
	global_load_dwordx4 v[14:17], v[2:3], off offset:16
	global_load_dwordx4 v[98:101], v[2:3], off
	s_nop 0
	global_load_dwordx4 v[2:5], v[6:7], off offset:16
	s_nop 0
	global_load_dwordx4 v[6:9], v[6:7], off
	v_ashrrev_i32_e32 v103, 31, v102
	v_lshlrev_b32_e32 v104, 16, v65
	v_and_b32_e32 v105, 0xffff0000, v65
	v_lshlrev_b64 v[102:103], 12, v[102:103]
	v_lshlrev_b32_e32 v106, 16, v64
	v_and_b32_e32 v107, 0xffff0000, v64
	v_lshlrev_b32_e32 v64, 16, v63
	v_and_b32_e32 v65, 0xffff0000, v63
	s_waitcnt vmcnt(22)
	v_pk_add_f32 v[18:19], v[186:187], v[104:105]
	v_lshlrev_b32_e32 v104, 16, v62
	v_and_b32_e32 v105, 0xffff0000, v62
	v_pk_add_f32 v[20:21], v[188:189], v[106:107]
	v_pk_add_f32 v[62:63], v[184:185], v[104:105]
	v_pk_add_f32 v[12:13], v[182:183], v[64:65]
	v_cvt_pk_bf16_f32 v10, v18, v19
	v_lshl_add_u64 v[18:19], s[0:1], 0, v[102:103]
	v_cvt_pk_bf16_f32 v11, v20, v21
	v_cvt_pk_bf16_f32 v12, v12, v13
	v_cvt_pk_bf16_f32 v13, v62, v63
	v_lshl_add_u64 v[18:19], v[18:19], 0, v[32:33]
	global_store_dwordx4 v[18:19], v[10:13], off
	v_lshlrev_b32_e32 v20, 16, v59
	v_and_b32_e32 v21, 0xffff0000, v59
	v_lshlrev_b32_e32 v10, 16, v61
	v_and_b32_e32 v11, 0xffff0000, v61
	v_lshlrev_b32_e32 v12, 16, v60
	v_and_b32_e32 v13, 0xffff0000, v60
	s_waitcnt vmcnt(21)
; __device__ __forceinline__ unsigned cvt_pk_bf16(float lo, float hi) { const f32x2 v = {lo, hi}; const bf16x2_t b = __builtin_convertvector(v, bf16x2_t); return __builtin_bit_cast(unsigned, b); }
; __device__ __forceinline__ float bflo(unsigned w) { return __uint_as_float(w << 16); }
; __device__ __forceinline__ float bfhi(unsigned w) { return __uint_as_float(w & 0xffff0000u); }
; #define PG8_BAR __builtin_amdgcn_s_barrier()
;     ...
;         if (!has_next) break;
; #pragma unroll
;         for (int a = 0; a < 2; ++a)
; #pragma unroll
;             for (int b = 0; b < 2; ++b)
; #pragma unroll
;                 for (int m = 0; m < 4; ++m)
; #pragma unroll
;                     for (int n = 0; n < 2; ++n) acc[a][b][m][n] = (f32x4){0.f, 0.f, 0.f, 0.f};
;         cur = nxt; cA = nA; cB = nB; ++ui;
;         if constexpr (GATHER) {
; #pragma unroll
;             for (int _h = 0; _h < 2; ++_h)
; #pragma unroll
;                 for (int _i = 0; _i < 2; ++_i) gC[_h][_i] = gN[_h][_i]; }
;         if constexpr (ALIGN_EPI) { if (wr == 1) PG8_BAR; }
;     __device__ __forceinline__ void operator()(AccRef acc, const Unit& u, int wr, int wc, int fr, int fq) const {
;     ...
; #pragma unroll
;             for (int m = 0; m < 4; ++m)
; #pragma unroll
;                 for (int bj = 0; bj < 2; ++bj) { const int row = u.pm * 256 + ai * 128 + wr * 64 + m * 16 + fr, col = colb + bj * 128; const u32x4 y = pk[ai][m][bj];
;                     const f32x4 x0 = xa[m][bj][0] + (f32x4){bflo(y.x), bfhi(y.x), bflo(y.y), bfhi(y.y)}, x1 = xa[m][bj][1] + (f32x4){bflo(y.z), bfhi(y.z), bflo(y.w), bfhi(y.w)};
;                     u32x4 w; w.x = cvt_pk_bf16(x0[0], x0[1]); w.y = cvt_pk_bf16(x0[2], x0[3]); w.z = cvt_pk_bf16(x1[0], x1[1]); w.w = cvt_pk_bf16(x1[2], x1[3]);
;                     *(u32x4*)(xo + (size_t)row * DM + col) = w; }
	v_pk_add_f32 v[10:11], v[194:195], v[10:11]
	v_lshlrev_b32_e32 v26, 16, v58
	v_and_b32_e32 v27, 0xffff0000, v58
	v_pk_add_f32 v[12:13], v[196:197], v[12:13]
	v_pk_add_f32 v[24:25], v[192:193], v[26:27]
	v_pk_add_f32 v[20:21], v[190:191], v[20:21]
	v_cvt_pk_bf16_f32 v10, v10, v11
	v_cvt_pk_bf16_f32 v11, v12, v13
	v_cvt_pk_bf16_f32 v12, v20, v21
	v_cvt_pk_bf16_f32 v13, v24, v25
	global_store_dwordx4 v[18:19], v[10:13], off offset:256
	v_lshlrev_b32_e32 v20, 16, v55
	v_and_b32_e32 v21, 0xffff0000, v55
	v_add_u32_e32 v10, 0x90, v30
	v_ashrrev_i32_e32 v11, 31, v10
	v_lshlrev_b64 v[18:19], 12, v[10:11]
	v_lshlrev_b32_e32 v10, 16, v57
	v_and_b32_e32 v11, 0xffff0000, v57
	v_lshlrev_b32_e32 v12, 16, v56
	v_and_b32_e32 v13, 0xffff0000, v56
	v_lshlrev_b32_e32 v22, 16, v54
	v_and_b32_e32 v23, 0xffff0000, v54
	s_waitcnt vmcnt(20)
	v_pk_add_f32 v[12:13], v[204:205], v[12:13]
	v_pk_add_f32 v[10:11], v[202:203], v[10:11]
	v_pk_add_f32 v[22:23], v[200:201], v[22:23]
	v_pk_add_f32 v[20:21], v[198:199], v[20:21]
	v_lshl_add_u64 v[18:19], s[0:1], 0, v[18:19]
	v_cvt_pk_bf16_f32 v10, v10, v11
	v_cvt_pk_bf16_f32 v11, v12, v13
	v_cvt_pk_bf16_f32 v12, v20, v21
	v_cvt_pk_bf16_f32 v13, v22, v23
	v_lshl_add_u64 v[18:19], v[18:19], 0, v[32:33]
	global_store_dwordx4 v[18:19], v[10:13], off
	v_lshlrev_b32_e32 v20, 16, v51
	v_and_b32_e32 v21, 0xffff0000, v51
	v_lshlrev_b32_e32 v10, 16, v53
	v_and_b32_e32 v11, 0xffff0000, v53
	v_lshlrev_b32_e32 v12, 16, v52
	v_and_b32_e32 v13, 0xffff0000, v52
	v_lshlrev_b32_e32 v22, 16, v50
	v_and_b32_e32 v23, 0xffff0000, v50
	s_waitcnt vmcnt(19)
	v_pk_add_f32 v[12:13], v[222:223], v[12:13]
	v_pk_add_f32 v[10:11], v[220:221], v[10:11]
	v_pk_add_f32 v[22:23], v[218:219], v[22:23]
	v_pk_add_f32 v[20:21], v[216:217], v[20:21]
	v_cvt_pk_bf16_f32 v10, v10, v11
	v_cvt_pk_bf16_f32 v11, v12, v13
	v_cvt_pk_bf16_f32 v12, v20, v21
	v_cvt_pk_bf16_f32 v13, v22, v23
	global_store_dwordx4 v[18:19], v[10:13], off offset:256
	v_lshlrev_b32_e32 v20, 16, v47
	v_and_b32_e32 v21, 0xffff0000, v47
	v_add_u32_e32 v10, 0xa0, v30
	v_ashrrev_i32_e32 v11, 31, v10
	v_lshlrev_b64 v[18:19], 12, v[10:11]
	v_lshlrev_b32_e32 v10, 16, v49
	v_and_b32_e32 v11, 0xffff0000, v49
	v_lshlrev_b32_e32 v12, 16, v48
	v_and_b32_e32 v13, 0xffff0000, v48
	v_lshlrev_b32_e32 v22, 16, v46
	v_and_b32_e32 v23, 0xffff0000, v46
	s_waitcnt vmcnt(18)
	v_pk_add_f32 v[12:13], v[230:231], v[12:13]
	v_pk_add_f32 v[10:11], v[228:229], v[10:11]
	v_pk_add_f32 v[22:23], v[226:227], v[22:23]
	v_pk_add_f32 v[20:21], v[224:225], v[20:21]
	v_lshl_add_u64 v[18:19], s[0:1], 0, v[18:19]
	v_cvt_pk_bf16_f32 v10, v10, v11
	v_cvt_pk_bf16_f32 v11, v12, v13
	v_cvt_pk_bf16_f32 v12, v20, v21
	v_cvt_pk_bf16_f32 v13, v22, v23
	v_lshl_add_u64 v[18:19], v[18:19], 0, v[32:33]
	global_store_dwordx4 v[18:19], v[10:13], off
	v_lshlrev_b32_e32 v20, 16, v43
	v_and_b32_e32 v21, 0xffff0000, v43
	v_lshlrev_b32_e32 v10, 16, v45
	v_and_b32_e32 v11, 0xffff0000, v45
	v_lshlrev_b32_e32 v12, 16, v44
	v_and_b32_e32 v13, 0xffff0000, v44
	v_lshlrev_b32_e32 v22, 16, v42
	v_and_b32_e32 v23, 0xffff0000, v42
	s_waitcnt vmcnt(17)
	v_pk_add_f32 v[12:13], v[238:239], v[12:13]
	v_pk_add_f32 v[10:11], v[236:237], v[10:11]
	v_pk_add_f32 v[22:23], v[234:235], v[22:23]
	v_pk_add_f32 v[20:21], v[232:233], v[20:21]
	v_cvt_pk_bf16_f32 v10, v10, v11
	v_cvt_pk_bf16_f32 v11, v12, v13
	v_cvt_pk_bf16_f32 v12, v20, v21
	v_cvt_pk_bf16_f32 v13, v22, v23
	global_store_dwordx4 v[18:19], v[10:13], off offset:256
	v_lshlrev_b32_e32 v20, 16, v39
	v_and_b32_e32 v21, 0xffff0000, v39
	v_add_u32_e32 v10, 0xb0, v30
	v_ashrrev_i32_e32 v11, 31, v10
	v_lshlrev_b64 v[18:19], 12, v[10:11]
	v_lshlrev_b32_e32 v10, 16, v41
	v_and_b32_e32 v11, 0xffff0000, v41
	v_lshlrev_b32_e32 v12, 16, v40
	v_and_b32_e32 v13, 0xffff0000, v40
	s_waitcnt vmcnt(8)
	v_pk_add_f32 v[12:13], v[100:101], v[12:13]
	v_pk_add_f32 v[10:11], v[98:99], v[10:11]
	v_lshlrev_b32_e32 v22, 16, v38
	v_and_b32_e32 v23, 0xffff0000, v38
	v_pk_add_f32 v[14:15], v[14:15], v[20:21]
	v_pk_add_f32 v[16:17], v[16:17], v[22:23]
	v_cvt_pk_bf16_f32 v10, v10, v11
	v_cvt_pk_bf16_f32 v11, v12, v13
	v_cvt_pk_bf16_f32 v12, v14, v15
	v_lshl_add_u64 v[14:15], s[0:1], 0, v[18:19]
	v_cvt_pk_bf16_f32 v13, v16, v17
	v_lshl_add_u64 v[14:15], v[14:15], 0, v[32:33]
	global_store_dwordx4 v[14:15], v[10:13], off
	s_mov_b64 s[0:1], -1
	s_nop 0
	v_lshlrev_b32_e32 v10, 16, v37
	v_and_b32_e32 v11, 0xffff0000, v37
	v_lshlrev_b32_e32 v12, 16, v36
	v_and_b32_e32 v13, 0xffff0000, v36
	s_waitcnt vmcnt(7)
	v_pk_add_f32 v[8:9], v[8:9], v[12:13]
	v_pk_add_f32 v[6:7], v[6:7], v[10:11]
	v_lshlrev_b32_e32 v10, 16, v35
	v_and_b32_e32 v11, 0xffff0000, v35
	v_lshlrev_b32_e32 v12, 16, v34
	v_and_b32_e32 v13, 0xffff0000, v34
	v_pk_add_f32 v[12:13], v[4:5], v[12:13]
	v_pk_add_f32 v[4:5], v[2:3], v[10:11]
	v_cvt_pk_bf16_f32 v2, v6, v7
	v_cvt_pk_bf16_f32 v3, v8, v9
	v_cvt_pk_bf16_f32 v4, v4, v5
	v_cvt_pk_bf16_f32 v5, v12, v13
	global_store_dwordx4 v[14:15], v[2:5], off offset:256
	s_cbranch_vccnz .LBB0_1665
	s_andn2_b64 vcc, exec, s[2:3]
	s_cbranch_vccnz .LBB0_1664
	s_barrier
	s_branch .LBB0_1664
